# baseline (speedup 1.0000x reference)
_Z7gemm_x3ILi2ELi2ELi2ELi0EEvPKcS1_iiPKfiS3_PKiPciPy:
	s_load_dwordx8 s[4:11], s[0:1], 0x0
	s_ashr_i32 s17, s2, 3
	s_abs_i32 s18, s17
	v_lshlrev_b32_e32 v170, 4, v0
	s_load_dword s16, s[0:1], 0x20
	s_load_dwordx4 s[12:15], s[0:1], 0x28
	s_waitcnt lgkmcnt(0)
	s_abs_i32 s3, s9
	v_cvt_f32_u32_e32 v2, s3
	s_sub_i32 s20, 0, s3
	s_xor_b32 s19, s17, s9
	s_ashr_i32 s19, s19, 31
	v_rcp_iflag_f32_e32 v2, v2
	v_bfe_u32 v19, v0, 6, 1
	v_and_b32_e32 v164, 31, v0
	v_mov_b32_e32 v155, 0
	v_mul_f32_e32 v2, 0x4f7ffffe, v2
	v_cvt_u32_f32_e32 v2, v2
	v_lshlrev_b32_e32 v165, 6, v19
	v_mov_b32_e32 v3, v155
	v_bfe_u32 v1, v0, 7, 1
	v_readfirstlane_b32 s21, v2
	s_mul_i32 s20, s20, s21
	s_mul_hi_u32 s20, s21, s20
	s_add_i32 s21, s21, s20
	s_mul_hi_u32 s20, s18, s21
	s_mul_i32 s21, s20, s3
	s_sub_i32 s18, s18, s21
	s_add_i32 s22, s20, 1
	s_sub_i32 s21, s18, s3
	s_cmp_ge_u32 s18, s3
	s_cselect_b32 s20, s22, s20
	s_cselect_b32 s18, s21, s18
	s_add_i32 s21, s20, 1
	s_cmp_ge_u32 s18, s3
	s_cselect_b32 s3, s21, s20
	s_xor_b32 s3, s3, s19
	s_sub_i32 s20, s3, s19
	s_mul_i32 s3, s20, s9
	s_sub_i32 s3, s17, s3
	s_lshl_b32 s2, s2, 7
	s_lshl_b32 s3, s3, 10
	s_and_b32 s2, s2, 0x380
	s_or_b32 s17, s3, s2
	s_ashr_i32 s9, s17, 7
	s_ashr_i32 s2, s8, 6
	s_ashr_i32 s18, s9, 31
	s_ashr_i32 s3, s2, 31
	s_lshl_b32 s21, s2, 14
	s_mul_i32 s18, s21, s18
	s_mul_hi_u32 s19, s21, s9
	s_lshr_b64 s[2:3], s[2:3], 18
	s_add_i32 s18, s19, s18
	s_mul_i32 s3, s2, s9
	s_add_i32 s3, s18, s3
	s_mul_i32 s9, s21, s9
	s_add_u32 s18, s6, s9
	s_addc_u32 s19, s7, s3
	s_movk_i32 s3, 0x70
	v_bitop3_b32 v154, v0, s3, v170 bitop3:0x48
	s_ashr_i32 s3, s20, 31
	s_mul_i32 s3, s21, s3
	s_mul_hi_u32 s6, s21, s20
	s_add_i32 s3, s6, s3
	s_mul_i32 s2, s2, s20
	s_add_i32 s6, s3, s2
	s_mul_i32 s7, s21, s20
	s_add_u32 s2, s4, s7
	s_addc_u32 s3, s5, s6
	v_and_b32_e32 v2, 0x1f80, v170
	v_or3_b32 v6, v165, s17, v164
	v_lshl_add_u64 v[4:5], s[2:3], 0, v[2:3]
	v_ashrrev_i32_e32 v7, 31, v6
	v_lshl_add_u64 v[146:147], v[4:5], 0, v[154:155]
	s_movk_i32 s9, 0x3f80
	v_mov_b32_e32 v4, 0x2000
	v_lshrrev_b32_e32 v168, 8, v0
	v_bfe_u32 v18, v0, 5, 1
	v_lshl_add_u64 v[6:7], v[6:7], 2, s[14:15]
	v_lshlrev_b32_e32 v166, 6, v1
	v_bitop3_b32 v4, v170, s9, v4 bitop3:0xc8
	global_load_dword v20, v[6:7], off
	global_load_dword v21, v[6:7], off offset:128
	s_lshl_b32 s9, s20, 7
	v_lshl_or_b32 v6, v168, 5, v166
	v_lshlrev_b32_e32 v167, 2, v18
	v_or3_b32 v14, v6, v167, s9
	v_cmp_gt_i32_e32 vcc, s16, v14
	v_or_b32_e32 v10, 8, v14
	v_mov_b32_e32 v5, v155
	v_cndmask_b32_e32 v6, 0, v14, vcc
	v_cmp_gt_i32_e32 vcc, s16, v10
	v_ashrrev_i32_e32 v7, 31, v6
	v_lshlrev_b64 v[6:7], 2, v[6:7]
	v_cndmask_b32_e32 v10, 0, v10, vcc
	v_ashrrev_i32_e32 v11, 31, v10
	v_lshl_add_u64 v[8:9], s[10:11], 0, v[6:7]
	v_lshlrev_b64 v[10:11], 2, v[10:11]
	v_lshl_add_u64 v[12:13], s[10:11], 0, v[10:11]
	global_load_dwordx4 v[78:81], v[8:9], off
	global_load_dwordx4 v[74:77], v[12:13], off
	v_or_b32_e32 v8, 16, v14
	v_cmp_gt_i32_e32 vcc, s16, v8
	v_or_b32_e32 v14, 24, v14
	v_lshl_add_u64 v[156:157], s[2:3], 0, v[4:5]
	s_movk_i32 s2, 0x7f80
	v_mov_b32_e32 v4, 0x6000
	v_cndmask_b32_e32 v8, 0, v8, vcc
	v_cmp_gt_i32_e32 vcc, s16, v14
	v_bitop3_b32 v4, v170, s2, v4 bitop3:0xc8
	v_ashrrev_i32_e32 v9, 31, v8
	v_cndmask_b32_e32 v14, 0, v14, vcc
	v_lshl_add_u64 v[160:161], s[18:19], 0, v[4:5]
	s_movk_i32 s2, 0xc000
	v_lshlrev_b64 v[8:9], 2, v[8:9]
	v_ashrrev_i32_e32 v15, 31, v14
	v_lshl_add_u64 v[4:5], v[160:161], 0, v[154:155]
	s_mov_b32 s3, -1
	v_lshl_add_u64 v[12:13], s[10:11], 0, v[8:9]
	v_lshlrev_b64 v[14:15], 2, v[14:15]
	v_add_u32_e32 v178, 0, v170
	v_lshl_add_u64 v[152:153], v[4:5], 0, s[2:3]
	v_lshl_add_u64 v[16:17], s[10:11], 0, v[14:15]
	global_load_dwordx4 v[70:73], v[12:13], off
	global_load_dwordx4 v[66:69], v[16:17], off
	v_readfirstlane_b32 s2, v178
	v_add_u32_e32 v12, 0x2000, v178
	s_mov_b32 m0, s2
	v_readfirstlane_b32 s2, v12
	v_add_u32_e32 v12, 0x4000, v178
	v_lshl_add_u64 v[150:151], v[156:157], 0, v[154:155]
	v_lshl_add_u64 v[158:159], s[18:19], 0, v[2:3]
	global_load_lds_dwordx4 v[146:147], off
	s_mov_b32 m0, s2
	v_readfirstlane_b32 s2, v12
	v_add_u32_e32 v12, 0x6000, v178
	v_lshl_add_u64 v[148:149], v[158:159], 0, v[154:155]
	global_load_lds_dwordx4 v[150:151], off
	s_mov_b32 m0, s2
	v_readfirstlane_b32 s2, v12
	v_add_u32_e32 v16, 0x8000, v178
	global_load_lds_dwordx4 v[148:149], off
	s_mov_b32 m0, s2
	s_mov_b64 s[10:11], 0x4000
	v_readfirstlane_b32 s2, v16
	v_add_u32_e32 v16, 0xa000, v178
	global_load_lds_dwordx4 v[152:153], off
	v_lshl_add_u64 v[12:13], v[146:147], 0, s[10:11]
	s_mov_b32 m0, s2
	v_readfirstlane_b32 s2, v16
	v_add_u32_e32 v16, 0xc000, v178
	global_load_lds_dwordx4 v[12:13], off
	v_lshl_add_u64 v[12:13], v[150:151], 0, s[10:11]
	s_mov_b32 m0, s2
	v_readfirstlane_b32 s2, v16
	global_load_lds_dwordx4 v[12:13], off
	v_lshl_add_u64 v[12:13], v[148:149], 0, s[10:11]
	s_mov_b32 m0, s2
	v_lshlrev_b32_e32 v169, 13, v19
	global_load_lds_dwordx4 v[12:13], off
	v_add_u32_e32 v12, 0xe000, v178
	s_nop 0
	v_readfirstlane_b32 s2, v12
	s_mov_b32 m0, s2
	s_add_i32 s2, 0, 0x10000
	v_add_u32_e32 v16, s2, v170
	s_mov_b64 s[2:3], 0x8000
	v_readfirstlane_b32 s14, v16
	v_add_u32_e32 v17, 0x2000, v16
	global_load_lds_dwordx4 v[4:5], off
	v_lshl_add_u64 v[12:13], v[146:147], 0, s[2:3]
	s_mov_b32 m0, s14
	v_readfirstlane_b32 s14, v17
	v_add_u32_e32 v17, 0x4000, v16
	global_load_lds_dwordx4 v[12:13], off
	v_lshl_add_u64 v[12:13], v[150:151], 0, s[2:3]
	s_mov_b32 m0, s14
	v_readfirstlane_b32 s14, v17
	global_load_lds_dwordx4 v[12:13], off
	v_lshl_add_u64 v[12:13], v[148:149], 0, s[2:3]
	s_mov_b32 m0, s14
	v_lshl_add_u64 v[4:5], v[4:5], 0, s[10:11]
	global_load_lds_dwordx4 v[12:13], off
	v_add_u32_e32 v12, 0x6000, v16
	s_mov_b32 s14, 0
	v_readfirstlane_b32 s10, v12
	s_mov_b32 m0, s10
	s_load_dwordx2 s[10:11], s[0:1], 0x38
	global_load_lds_dwordx4 v[4:5], off
	s_mov_b64 s[24:25], 0xc000
	v_add_u32_e32 v180, 0x18000, v170
	v_add_u32_e32 v181, 0x1a000, v170
	v_add_u32_e32 v182, 0x1c000, v170
	v_add_u32_e32 v183, 0x1e000, v170
	v_lshl_add_u64 v[12:13], v[146:147], 0, s[24:25]
	v_lshl_add_u64 v[16:17], v[150:151], 0, s[24:25]
	v_readfirstlane_b32 s26, v180
	v_readfirstlane_b32 s27, v181
	v_readfirstlane_b32 s28, v182
	v_readfirstlane_b32 s29, v183
	s_mov_b32 m0, s26
	v_lshl_add_u64 v[184:185], v[148:149], 0, s[24:25]
	global_load_lds_dwordx4 v[12:13], off
	s_mov_b32 m0, s27
	v_lshl_add_u64 v[186:187], v[152:153], 0, s[24:25]
	global_load_lds_dwordx4 v[16:17], off
	s_mov_b32 m0, s28
	s_nop 0
	global_load_lds_dwordx4 v[184:185], off
	s_mov_b32 m0, s29
	s_nop 0
	global_load_lds_dwordx4 v[186:187], off
	v_lshlrev_b32_e32 v4, 2, v168
	v_bfe_u32 v5, v0, 1, 3
	v_bitop3_b32 v4, v4, v5, v18 bitop3:0x36
	v_lshlrev_b32_e32 v22, 4, v4
	v_lshlrev_b32_e32 v4, 7, v164
	v_lshl_or_b32 v5, v1, 13, v4
	v_or_b32_e32 v24, v169, v4
	v_add_u32_e32 v171, v5, v22
	v_or_b32_e32 v5, 0x4000, v22
	v_or_b32_e32 v26, 0x1000, v24
	v_add_u32_e32 v23, 0x1000, v171
	v_add_u32_e32 v25, v5, v24
	v_add_u32_e32 v27, v5, v26
	s_waitcnt vmcnt(12)
	s_barrier
	v_add_u32_e32 v12, 0x800, v20
	s_movk_i32 s15, 0xfa0
	v_mov_b64_e32 v[4:5], s[12:13]
	v_mad_i64_i32 v[12:13], s[12:13], v12, s15, v[4:5]
	v_lshl_add_u64 v[16:17], v[12:13], 0, v[6:7]
	v_lshl_add_u64 v[18:19], v[12:13], 0, v[10:11]
	global_load_dwordx4 v[110:113], v[16:17], off
	global_load_dwordx4 v[106:109], v[18:19], off
	v_lshl_add_u64 v[16:17], v[12:13], 0, v[8:9]
	v_lshl_add_u64 v[12:13], v[12:13], 0, v[14:15]
	global_load_dwordx4 v[102:105], v[16:17], off
	global_load_dwordx4 v[98:101], v[12:13], off
	v_add_u32_e32 v12, 0x800, v21
	v_mad_i64_i32 v[4:5], s[12:13], v12, s15, v[4:5]
	v_lshl_add_u64 v[6:7], v[4:5], 0, v[6:7]
	v_lshl_add_u64 v[10:11], v[4:5], 0, v[10:11]
	global_load_dwordx4 v[94:97], v[6:7], off
	global_load_dwordx4 v[90:93], v[10:11], off
	v_lshl_add_u64 v[6:7], v[4:5], 0, v[8:9]
	v_lshl_add_u64 v[4:5], v[4:5], 0, v[14:15]
	global_load_dwordx4 v[86:89], v[6:7], off
	global_load_dwordx4 v[82:85], v[4:5], off
	v_add_u32_e32 v4, 0, v171
	v_add_u32_e32 v172, v22, v24
	ds_read_b128 v[130:133], v4
	ds_read_b128 v[126:129], v4 offset:4096
	v_add_u32_e32 v4, 0, v172
	v_add_u32_e32 v174, v22, v26
	v_xor_b32_e32 v177, 32, v171
	v_add_u32_e32 v5, 0, v174
	ds_read_b128 v[142:145], v4 offset:16384
	ds_read_b128 v[138:141], v5 offset:16384
	v_add_u32_e32 v4, 0, v177
	v_xor_b32_e32 v175, 32, v23
	v_xor_b32_e32 v173, 32, v25
	v_xor_b32_e32 v176, 32, v27
	v_add_u32_e32 v5, 0, v175
	v_add_u32_e32 v6, 0, v173
	v_add_u32_e32 v7, 0, v176
	ds_read_b128 v[134:137], v4
	ds_read_b128 v[114:117], v5
	ds_read_b128 v[122:125], v6
	ds_read_b128 v[118:121], v7
	s_cmpk_lt_i32 s8, 0x140
	s_cbranch_scc1 .LBB5_3
	s_ashr_i32 s12, s8, 31
	s_lshr_b32 s12, s12, 26
	s_add_i32 s8, s8, s12
	s_ashr_i32 s8, s8, 6
	s_add_i32 s8, s8, -4
	s_add_u32 s4, s4, s7
	s_addc_u32 s5, s5, s6
	v_lshl_add_u64 v[162:163], s[4:5], 0, v[2:3]
	s_mov_b64 s[24:25], 0x4000
	v_lshl_add_u64 v[162:163], v[162:163], 0, s[24:25]
	v_lshl_add_u64 v[156:157], v[156:157], 0, s[24:25]
	v_lshl_add_u64 v[158:159], v[158:159], 0, s[24:25]
	v_lshl_add_u64 v[160:161], v[160:161], 0, s[24:25]
	v_mov_b32_e32 v2, 0
	s_mov_b32 s12, 0x18000
	s_mov_b64 s[4:5], 0xc000
	s_mov_b64 s[6:7], 0x10000
	v_mov_b32_e32 v3, v2
	v_mov_b32_e32 v4, v2
	v_mov_b32_e32 v5, v2
	v_mov_b32_e32 v6, v2
	v_mov_b32_e32 v7, v2
	v_mov_b32_e32 v8, v2
	v_mov_b32_e32 v9, v2
	v_mov_b32_e32 v10, v2
	v_mov_b32_e32 v11, v2
	v_mov_b32_e32 v12, v2
	v_mov_b32_e32 v13, v2
	v_mov_b32_e32 v14, v2
	v_mov_b32_e32 v15, v2
	v_mov_b32_e32 v16, v2
	v_mov_b32_e32 v17, v2
	v_mov_b32_e32 v18, v2
	v_mov_b32_e32 v19, v2
	v_mov_b32_e32 v20, v2
	v_mov_b32_e32 v21, v2
	v_mov_b32_e32 v22, v2
	v_mov_b32_e32 v23, v2
	v_mov_b32_e32 v24, v2
	v_mov_b32_e32 v25, v2
	v_mov_b32_e32 v26, v2
	v_mov_b32_e32 v27, v2
	v_mov_b32_e32 v28, v2
	v_mov_b32_e32 v29, v2
	v_mov_b32_e32 v30, v2
	v_mov_b32_e32 v31, v2
	v_mov_b32_e32 v32, v2
	v_mov_b32_e32 v33, v2
	v_mov_b32_e32 v34, v2
	v_mov_b32_e32 v35, v2
	v_mov_b32_e32 v36, v2
	v_mov_b32_e32 v37, v2
	v_mov_b32_e32 v38, v2
	v_mov_b32_e32 v39, v2
	v_mov_b32_e32 v40, v2
	v_mov_b32_e32 v41, v2
	v_mov_b32_e32 v42, v2
	v_mov_b32_e32 v43, v2
	v_mov_b32_e32 v44, v2
	v_mov_b32_e32 v45, v2
	v_mov_b32_e32 v46, v2
	v_mov_b32_e32 v47, v2
	v_mov_b32_e32 v48, v2
	v_mov_b32_e32 v49, v2
	v_mov_b32_e32 v50, v2
	v_mov_b32_e32 v51, v2
	v_mov_b32_e32 v52, v2
	v_mov_b32_e32 v53, v2
	v_mov_b32_e32 v54, v2
	v_mov_b32_e32 v55, v2
	v_mov_b32_e32 v56, v2
	v_mov_b32_e32 v57, v2
	v_mov_b32_e32 v58, v2
	v_mov_b32_e32 v59, v2
	v_mov_b32_e32 v60, v2
	v_mov_b32_e32 v61, v2
	v_mov_b32_e32 v62, v2
	v_mov_b32_e32 v63, v2
	v_mov_b32_e32 v64, v2
	v_mov_b32_e32 v65, v2
	v_readfirstlane_b32 s26, v0
	s_nop 3
	s_lshr_b32 s26, s26, 6
	s_cmp_ge_u32 s26, 4
	s_cbranch_scc0 .Lg1_prio_done
	s_setprio 1
.Lg1_prio_done:
.LBB5_2:
	s_waitcnt vmcnt(8) lgkmcnt(0)
	s_barrier
	v_mfma_f32_32x32x16_f16 v[50:65], v[130:133], v[142:145], v[50:65]
	s_add_i32 s13, s12, 0xfffe8000
	s_and_b32 s13, s13, 0x10000
	s_add_i32 s15, s13, 0
	s_add_i32 s26, s12, 0x8000
	s_and_b32 s26, s26, 0x18000
	v_add_u32_e32 v202, s26, v178
	v_lshl_add_u64 v[192:193], v[162:163], 0, v[154:155]
	v_add_u32_e32 v203, 0x2000, v202
	v_lshl_add_u64 v[200:201], v[192:193], 0, s[4:5]
	v_mfma_f32_32x32x16_f16 v[34:49], v[130:133], v[138:141], v[34:49]
	v_add_u32_e32 v130, s15, v171
	v_readfirstlane_b32 s26, v202
	v_readfirstlane_b32 s27, v203
	v_lshl_add_u64 v[194:195], v[156:157], 0, v[154:155]
	s_mov_b32 m0, s26
	v_add_u32_e32 v204, 0x4000, v202
	global_load_lds_dwordx4 v[200:201], off
	v_mfma_f32_32x32x16_f16 v[18:33], v[126:129], v[142:145], v[18:33]
	v_add_u32_e32 v142, s15, v177
	v_add_u32_e32 v143, s15, v175
	v_lshl_add_u64 v[200:201], v[194:195], 0, s[4:5]
	s_mov_b32 m0, s27
	v_readfirstlane_b32 s28, v204
	global_load_lds_dwordx4 v[200:201], off
	v_mfma_f32_32x32x16_f16 v[2:17], v[126:129], v[138:141], v[2:17]
	v_add_u32_e32 v138, s15, v174
	ds_read_b128 v[126:129], v130 offset:32768
	ds_read_b128 v[130:133], v130 offset:36864
	v_mfma_f32_32x32x16_f16 v[50:65], v[134:137], v[122:125], v[50:65]
	v_lshl_add_u64 v[196:197], v[158:159], 0, v[154:155]
	v_add_u32_e32 v205, 0x6000, v202
	v_lshl_add_u64 v[200:201], v[196:197], 0, s[4:5]
	s_mov_b32 m0, s28
	v_mfma_f32_32x32x16_f16 v[34:49], v[134:137], v[118:121], v[34:49]
	v_add_u32_e32 v134, s15, v172
	ds_read_b128 v[134:137], v134 offset:49152
	ds_read_b128 v[138:141], v138 offset:49152
	global_load_lds_dwordx4 v[200:201], off
	v_readfirstlane_b32 s29, v205
	v_mfma_f32_32x32x16_f16 v[18:33], v[114:117], v[122:125], v[18:33]
	ds_read_b128 v[122:125], v142 offset:32768
	ds_read_b128 v[180:183], v143 offset:32768
	v_add_u32_e32 v142, s15, v173
	v_add_u32_e32 v143, s15, v176
	ds_read_b128 v[184:187], v142 offset:32768
	ds_read_b128 v[188:191], v143 offset:32768
	v_lshl_add_u64 v[198:199], v[160:161], 0, v[154:155]
	v_lshl_add_u64 v[200:201], v[198:199], 0, s[2:3]
	s_mov_b32 m0, s29
	v_mfma_f32_32x32x16_f16 v[2:17], v[114:117], v[118:121], v[2:17]
	global_load_lds_dwordx4 v[200:201], off
	s_waitcnt vmcnt(8) lgkmcnt(0)
	s_barrier
	v_mfma_f32_32x32x16_f16 v[50:65], v[126:129], v[134:137], v[50:65]
	s_xor_b32 s15, s13, 0x10000
	s_add_i32 s15, s15, 0
	s_add_i32 s26, s13, 0x8000
	v_add_u32_e32 v202, s26, v178
	v_lshl_add_u64 v[200:201], v[192:193], 0, s[6:7]
	v_add_u32_e32 v114, s15, v171
	v_add_u32_e32 v115, s15, v174
	v_add_u32_e32 v118, s15, v173
	v_add_u32_e32 v119, s15, v176
	v_add_u32_e32 v203, 0x2000, v202
	v_readfirstlane_b32 s26, v202
	v_mfma_f32_32x32x16_f16 v[34:49], v[126:129], v[138:141], v[34:49]
	s_mov_b32 m0, s26
	v_readfirstlane_b32 s27, v203
	v_add_u32_e32 v204, 0x4000, v202
	global_load_lds_dwordx4 v[200:201], off
	v_mfma_f32_32x32x16_f16 v[18:33], v[130:133], v[134:137], v[18:33]
	v_lshl_add_u64 v[200:201], v[194:195], 0, s[6:7]
	s_mov_b32 m0, s27
	v_readfirstlane_b32 s28, v204
	global_load_lds_dwordx4 v[200:201], off
	v_mfma_f32_32x32x16_f16 v[2:17], v[130:133], v[138:141], v[2:17]
	ds_read_b128 v[130:133], v114
	ds_read_b128 v[126:129], v114 offset:4096
	v_add_u32_e32 v114, s15, v172
	ds_read_b128 v[142:145], v114 offset:16384
	ds_read_b128 v[138:141], v115 offset:16384
	v_add_u32_e32 v114, s15, v177
	v_add_u32_e32 v115, s15, v175
	ds_read_b128 v[134:137], v114
	ds_read_b128 v[114:117], v115
	v_mfma_f32_32x32x16_f16 v[50:65], v[122:125], v[184:187], v[50:65]
	v_lshl_add_u64 v[200:201], v[196:197], 0, s[6:7]
	v_add_u32_e32 v205, 0x6000, v202
	s_mov_b32 m0, s28
	v_mfma_f32_32x32x16_f16 v[34:49], v[122:125], v[188:191], v[34:49]
	ds_read_b128 v[122:125], v118
	ds_read_b128 v[118:121], v119
	global_load_lds_dwordx4 v[200:201], off
	v_readfirstlane_b32 s29, v205
	v_mfma_f32_32x32x16_f16 v[18:33], v[180:183], v[184:187], v[18:33]
	v_lshl_add_u64 v[200:201], v[198:199], 0, s[4:5]
	s_mov_b32 m0, s29
	v_mfma_f32_32x32x16_f16 v[2:17], v[180:183], v[188:191], v[2:17]
	global_load_lds_dwordx4 v[200:201], off
	s_add_i32 s14, s14, 2
	s_add_i32 s12, s12, 0x10000
	v_lshl_add_u64 v[162:163], v[162:163], 0, s[2:3]
	v_lshl_add_u64 v[156:157], v[156:157], 0, s[2:3]
	v_lshl_add_u64 v[158:159], v[158:159], 0, s[2:3]
	s_cmp_lt_i32 s14, s8
	v_lshl_add_u64 v[160:161], v[160:161], 0, s[2:3]
	s_cbranch_scc1 .LBB5_2
	s_branch .LBB5_4

_Z7gemm_x3ILi2ELi2ELi1ELi1EEvPKcS1_iiPKfiS3_PKiPciPy:
	s_load_dwordx8 s[4:11], s[0:1], 0x0
	s_ashr_i32 s17, s2, 3
	s_abs_i32 s15, s17
	v_lshlrev_b32_e32 v93, 4, v0
	v_mov_b32_e32 v81, 0
	s_waitcnt lgkmcnt(0)
	s_abs_i32 s3, s9
	v_cvt_f32_u32_e32 v1, s3
	s_xor_b32 s16, s17, s9
	s_ashr_i32 s18, s16, 31
	s_sub_i32 s16, 0, s3
	v_rcp_iflag_f32_e32 v2, v1
	v_mov_b64_e32 v[4:5], s[4:5]
	s_load_dword s14, s[0:1], 0x20
	s_load_dwordx2 s[12:13], s[0:1], 0x38
	v_bfe_u32 v1, v0, 7, 1
	v_mul_f32_e32 v2, 0x4f7ffffe, v2
	v_cvt_u32_f32_e32 v2, v2
	v_lshrrev_b32_e32 v90, 8, v0
	v_lshlrev_b32_e32 v88, 6, v1
	v_add_u32_e32 v99, 0, v93
	v_readfirstlane_b32 s19, v2
	s_mul_i32 s16, s16, s19
	s_mul_hi_u32 s16, s19, s16
	s_add_i32 s19, s19, s16
	s_mul_hi_u32 s16, s15, s19
	s_mul_i32 s19, s16, s3
	s_sub_i32 s15, s15, s19
	s_add_i32 s20, s16, 1
	s_sub_i32 s19, s15, s3
	s_cmp_ge_u32 s15, s3
	s_cselect_b32 s16, s20, s16
	s_cselect_b32 s15, s19, s15
	s_add_i32 s19, s16, 1
	s_cmp_ge_u32 s15, s3
	s_cselect_b32 s3, s19, s16
	s_xor_b32 s20, s3, s18
	s_sub_i32 s3, s20, s18
	s_mul_i32 s19, s3, s9
	s_lshl_b32 s15, s3, 7
	s_sub_i32 s3, s17, s19
	s_lshl_b32 s2, s2, 6
	s_lshl_b32 s3, s3, 9
	s_and_b32 s21, s2, 0x1c0
	s_ashr_i32 s9, s8, 31
	s_movk_i32 s2, 0x70
	v_lshrrev_b32_e32 v2, 3, v0
	s_or_b32 s16, s3, s21
	s_lshl_b32 s24, s8, 1
	v_bitop3_b32 v80, v0, s2, v93 bitop3:0x48
	v_or_b32_e32 v3, s15, v2
	s_lshr_b64 s[2:3], s[8:9], 31
	v_mul_lo_u32 v8, s2, v3
	v_mad_u64_u32 v[6:7], s[22:23], s24, v3, v[4:5]
	s_ashr_i32 s3, s15, 31
	v_or_b32_e32 v3, 0x200, v0
	s_mul_i32 s3, s24, s3
	v_lshrrev_b32_e32 v3, 3, v3
	s_add_i32 s25, s16, 0xffffff80
	v_add3_u32 v7, v8, v7, s3
	v_or_b32_e32 v3, s15, v3
	v_lshl_add_u64 v[74:75], v[6:7], 0, v[80:81]
	v_mul_lo_u32 v6, s2, v3
	v_mad_u64_u32 v[82:83], s[22:23], s24, v3, v[4:5]
	v_or_b32_e32 v3, s25, v2
	v_add_u32_e32 v3, 0x80, v3
	v_ashrrev_i32_e32 v4, 31, v3
	v_add3_u32 v83, v6, v83, s3
	v_mul_lo_u32 v6, s24, v4
	v_mov_b64_e32 v[4:5], s[6:7]
	v_mul_lo_u32 v7, s2, v3
	v_mad_u64_u32 v[4:5], s[2:3], s24, v3, v[4:5]
	v_add3_u32 v5, v7, v5, v6
	v_bfe_u32 v3, v0, 5, 1
	v_lshl_add_u64 v[78:79], v[4:5], 0, v[80:81]
	v_lshl_or_b32 v4, v90, 5, v88
	v_lshlrev_b32_e32 v89, 2, v3
	v_or3_b32 v8, v4, v89, s15
	s_waitcnt lgkmcnt(0)
	v_cmp_gt_i32_e32 vcc, s14, v8
	v_or_b32_e32 v6, 8, v8
	v_readfirstlane_b32 s2, v99
	v_cndmask_b32_e32 v4, 0, v8, vcc
	v_cmp_gt_i32_e32 vcc, s14, v6
	v_ashrrev_i32_e32 v5, 31, v4
	v_lshl_add_u64 v[4:5], v[4:5], 2, s[10:11]
	v_cndmask_b32_e32 v6, 0, v6, vcc
	v_ashrrev_i32_e32 v7, 31, v6
	v_lshl_add_u64 v[6:7], v[6:7], 2, s[10:11]
	global_load_dwordx4 v[46:49], v[4:5], off
	global_load_dwordx4 v[42:45], v[6:7], off
	v_or_b32_e32 v4, 16, v8
	v_cmp_gt_i32_e32 vcc, s14, v4
	v_or_b32_e32 v6, 24, v8
	s_mov_b32 m0, s2
	v_cndmask_b32_e32 v4, 0, v4, vcc
	v_cmp_gt_i32_e32 vcc, s14, v6
	v_ashrrev_i32_e32 v5, 31, v4
	v_lshl_add_u64 v[4:5], v[4:5], 2, s[10:11]
	v_cndmask_b32_e32 v6, 0, v6, vcc
	v_ashrrev_i32_e32 v7, 31, v6
	v_lshl_add_u64 v[6:7], v[6:7], 2, s[10:11]
	global_load_dwordx4 v[38:41], v[4:5], off
	global_load_dwordx4 v[34:37], v[6:7], off
	v_add_u32_e32 v4, 0x2000, v99
	v_lshl_add_u64 v[76:77], v[82:83], 0, v[80:81]
	v_readfirstlane_b32 s2, v4
	v_add_u32_e32 v4, 0x4000, v99
	global_load_lds_dwordx4 v[74:75], off
	s_mov_b32 m0, s2
	v_readfirstlane_b32 s2, v4
	v_add_u32_e32 v6, 0x6000, v99
	global_load_lds_dwordx4 v[76:77], off
	s_mov_b32 m0, s2
	s_mov_b64 s[2:3], 0x80
	v_readfirstlane_b32 s10, v6
	v_add_u32_e32 v6, 0x8000, v99
	global_load_lds_dwordx4 v[78:79], off
	v_lshl_add_u64 v[4:5], v[74:75], 0, s[2:3]
	s_mov_b32 m0, s10
	v_readfirstlane_b32 s10, v6
	global_load_lds_dwordx4 v[4:5], off
	v_lshl_add_u64 v[4:5], v[76:77], 0, s[2:3]
	s_mov_b32 m0, s10
	v_add_u32_e32 v6, 0xa000, v99
	global_load_lds_dwordx4 v[4:5], off
	v_lshl_add_u64 v[4:5], v[78:79], 0, s[2:3]
	v_readfirstlane_b32 s2, v6
	v_add_u32_e32 v6, 0xc000, v99
	s_mov_b32 m0, s2
	s_mov_b64 s[2:3], 0x100
	v_readfirstlane_b32 s10, v6
	v_add_u32_e32 v6, 0xe000, v99
	global_load_lds_dwordx4 v[4:5], off
	v_lshl_add_u64 v[4:5], v[74:75], 0, s[2:3]
	s_mov_b32 m0, s10
	v_readfirstlane_b32 s10, v6
	v_add_u32_e32 v6, 0x10000, v99
	global_load_lds_dwordx4 v[4:5], off
	v_lshl_add_u64 v[4:5], v[76:77], 0, s[2:3]
	s_mov_b32 m0, s10
	v_readfirstlane_b32 s10, v6
	global_load_lds_dwordx4 v[4:5], off
	v_lshl_add_u64 v[4:5], v[78:79], 0, s[2:3]
	s_mov_b32 m0, s10
	v_and_b32_e32 v91, 31, v0
	global_load_lds_dwordx4 v[4:5], off
	v_lshlrev_b32_e32 v4, 2, v90
	v_bfe_u32 v5, v0, 1, 3
	v_bitop3_b32 v3, v4, v5, v3 bitop3:0x36
	v_lshlrev_b32_e32 v4, 7, v91
	v_bfe_u32 v92, v0, 6, 1
	v_lshlrev_b32_e32 v3, 4, v3
	v_lshl_or_b32 v5, v1, 13, v4
	v_lshl_or_b32 v4, v92, 12, v4
	s_mov_b32 s10, 0
	v_add_u32_e32 v94, v5, v3
	v_add_u32_e32 v95, v4, v3
	v_add_u32_e32 v5, 0x1000, v94
	v_add_u32_e32 v3, 0x4000, v95
	s_waitcnt vmcnt(6)
	s_barrier
	v_add_u32_e32 v4, 0, v94
	ds_read_b128 v[66:69], v4
	ds_read_b128 v[62:65], v4 offset:4096
	v_add_u32_e32 v4, 0, v95
	v_xor_b32_e32 v96, 32, v94
	v_xor_b32_e32 v97, 32, v5
	v_add_u32_e32 v6, 0, v96
	ds_read_b128 v[70:73], v4 offset:16384
	ds_read_b128 v[58:61], v6
	v_add_u32_e32 v4, 0, v97
	v_xor_b32_e32 v98, 32, v3
	v_add_u32_e32 v3, 0, v98
	ds_read_b128 v[50:53], v4
	ds_read_b128 v[54:57], v3
	s_cmpk_lt_i32 s8, 0x140
	s_cbranch_scc1 .LBB6_3
	v_lshl_or_b32 v3, s20, 7, v2
	s_lshl_b32 s10, s18, 7
	v_subrev_u32_e32 v3, s10, v3
	v_mad_i64_i32 v[4:5], s[10:11], s8, v3, 0
	v_lshl_add_u64 v[84:85], v[4:5], 1, s[4:5]
	s_lshl_b32 s4, s17, 9
	s_or_b32 s4, s21, s4
	s_lshr_b32 s9, s9, 26
	v_add_u32_e32 v2, s4, v2
	s_lshl_b32 s4, s19, 9
	s_add_i32 s9, s8, s9
	v_subrev_u32_e32 v2, s4, v2
	s_ashr_i32 s9, s9, 6
	v_mad_i64_i32 v[2:3], s[4:5], s8, v2, 0
	v_mov_b32_e32 v18, 0
	s_add_i32 s9, s9, -4
	v_lshl_add_u64 v[86:87], v[2:3], 1, s[6:7]
	s_mov_b32 s10, 0
	s_mov_b64 s[4:5], 0x180
	s_mov_b64 s[6:7], 0x200
	v_mov_b32_e32 v19, v18
	v_mov_b32_e32 v20, v18
	v_mov_b32_e32 v21, v18
	v_mov_b32_e32 v22, v18
	v_mov_b32_e32 v23, v18
	v_mov_b32_e32 v24, v18
	v_mov_b32_e32 v25, v18
	v_mov_b32_e32 v26, v18
	v_mov_b32_e32 v27, v18
	v_mov_b32_e32 v28, v18
	v_mov_b32_e32 v29, v18
	v_mov_b32_e32 v30, v18
	v_mov_b32_e32 v31, v18
	v_mov_b32_e32 v32, v18
	v_mov_b32_e32 v33, v18
	v_mov_b32_e32 v2, v18
	v_mov_b32_e32 v3, v18
	v_mov_b32_e32 v4, v18
	v_mov_b32_e32 v5, v18
	v_mov_b32_e32 v6, v18
	v_mov_b32_e32 v7, v18
	v_mov_b32_e32 v8, v18
	v_mov_b32_e32 v9, v18
	v_mov_b32_e32 v10, v18
	v_mov_b32_e32 v11, v18
	v_mov_b32_e32 v12, v18
	v_mov_b32_e32 v13, v18
	v_mov_b32_e32 v14, v18
	v_mov_b32_e32 v15, v18
	v_mov_b32_e32 v16, v18
	v_mov_b32_e32 v17, v18
	v_readfirstlane_b32 s26, v0
	s_nop 3
	s_lshr_b32 s26, s26, 6
	s_cmp_ge_u32 s26, 4
	s_cbranch_scc0 .Lg2_prio_done
	s_setprio 1
.Lg2_prio_done:
.LBB6_2:
	s_waitcnt vmcnt(3) lgkmcnt(0)
	s_barrier
	v_mfma_f32_32x32x16_f16 v[18:33], v[66:69], v[70:73], v[18:33]
	s_and_b32 s8, s10, 2
	s_mul_i32 s11, s8, 0x6000
	s_add_i32 s17, s11, 0
	v_add_u32_e32 v66, s17, v94
	v_add_u32_e32 v100, s17, v97
	v_add_u32_e32 v104, s17, v98
	v_mfma_f32_32x32x16_f16 v[2:17], v[62:65], v[70:73], v[2:17]
	v_add_u32_e32 v70, s17, v95
	v_add_u32_e32 v71, s17, v96
	ds_read_b128 v[62:65], v66 offset:24576
	ds_read_b128 v[66:69], v66 offset:28672
	v_mfma_f32_32x32x16_f16 v[18:33], v[58:61], v[54:57], v[18:33]
	ds_read_b128 v[58:61], v70 offset:40960
	ds_read_b128 v[70:73], v71 offset:24576
	ds_read_b128 v[100:103], v100 offset:24576
	ds_read_b128 v[104:107], v104 offset:24576
	v_mfma_f32_32x32x16_f16 v[2:17], v[50:53], v[54:57], v[2:17]
	s_add_i32 s17, s10, -1
	s_and_b32 s17, s17, 3
	s_mulk_i32 s17, 0x6000
	v_add_u32_e32 v52, s17, v99
	v_lshl_add_u64 v[108:109], v[84:85], 0, v[80:81]
	v_readfirstlane_b32 s17, v52
	v_add_u32_e32 v53, 0x2000, v52
	v_lshl_add_u64 v[50:51], v[108:109], 0, s[4:5]
	s_mov_b32 m0, s17
	v_lshl_add_u64 v[110:111], v[82:83], 0, v[80:81]
	v_readfirstlane_b32 s17, v53
	v_add_u32_e32 v52, 0x4000, v52
	global_load_lds_dwordx4 v[50:51], off
	v_lshl_add_u64 v[50:51], v[110:111], 0, s[4:5]
	s_mov_b32 m0, s17
	v_lshl_add_u64 v[112:113], v[86:87], 0, v[80:81]
	v_readfirstlane_b32 s17, v52
	global_load_lds_dwordx4 v[50:51], off
	v_lshl_add_u64 v[50:51], v[112:113], 0, s[4:5]
	s_mov_b32 m0, s17
	s_nop 0
	global_load_lds_dwordx4 v[50:51], off
	s_waitcnt vmcnt(3) lgkmcnt(0)
	s_barrier
	v_mfma_f32_32x32x16_f16 v[18:33], v[62:65], v[58:61], v[18:33]
	s_xor_b32 s8, s8, 2
	s_mulk_i32 s8, 0x6000
	s_add_i32 s8, s8, 0
	v_add_u32_e32 v50, s8, v94
	v_add_u32_e32 v51, s8, v96
	v_add_u32_e32 v54, s8, v98
	v_mfma_f32_32x32x16_f16 v[2:17], v[66:69], v[58:61], v[2:17]
	ds_read_b128 v[66:69], v50
	ds_read_b128 v[62:65], v50 offset:4096
	v_add_u32_e32 v50, s8, v95
	v_mfma_f32_32x32x16_f16 v[18:33], v[70:73], v[104:107], v[18:33]
	ds_read_b128 v[70:73], v50 offset:16384
	ds_read_b128 v[58:61], v51
	v_add_u32_e32 v50, s8, v97
	ds_read_b128 v[50:53], v50
	ds_read_b128 v[54:57], v54
	v_mfma_f32_32x32x16_f16 v[2:17], v[100:103], v[104:107], v[2:17]
	v_add_u32_e32 v102, s11, v99
	v_add_u32_e32 v103, 0x2000, v102
	v_readfirstlane_b32 s8, v102
	v_lshl_add_u64 v[100:101], v[108:109], 0, s[6:7]
	s_mov_b32 m0, s8
	v_readfirstlane_b32 s8, v103
	v_add_u32_e32 v102, 0x4000, v102
	global_load_lds_dwordx4 v[100:101], off
	v_lshl_add_u64 v[100:101], v[110:111], 0, s[6:7]
	s_mov_b32 m0, s8
	v_readfirstlane_b32 s8, v102
	global_load_lds_dwordx4 v[100:101], off
	v_lshl_add_u64 v[100:101], v[112:113], 0, s[6:7]
	s_mov_b32 m0, s8
	s_add_i32 s10, s10, 2
	global_load_lds_dwordx4 v[100:101], off
	v_lshl_add_u64 v[84:85], v[84:85], 0, s[2:3]
	v_lshl_add_u64 v[82:83], v[82:83], 0, s[2:3]
	s_cmp_lt_i32 s10, s9
	v_lshl_add_u64 v[86:87], v[86:87], 0, s[2:3]
	s_cbranch_scc1 .LBB6_2
	s_branch .LBB6_4

	.amdhsa_kernel _Z7gemm_x3ILi2ELi2ELi1ELi1EEvPKcS1_iiPKfiS3_PKiPciPy
		.amdhsa_group_segment_fixed_size 0
		.amdhsa_private_segment_fixed_size 0
		.amdhsa_kernarg_size 80
		.amdhsa_user_sgpr_count 2
		.amdhsa_user_sgpr_dispatch_ptr 0
		.amdhsa_user_sgpr_queue_ptr 0
		.amdhsa_user_sgpr_kernarg_segment_ptr 1
		.amdhsa_user_sgpr_dispatch_id 0
		.amdhsa_user_sgpr_kernarg_preload_length 0
		.amdhsa_user_sgpr_kernarg_preload_offset 0
		.amdhsa_user_sgpr_private_segment_size 0
		.amdhsa_uses_dynamic_stack 0
		.amdhsa_enable_private_segment 0
		.amdhsa_system_sgpr_workgroup_id_x 1
		.amdhsa_system_sgpr_workgroup_id_y 0
		.amdhsa_system_sgpr_workgroup_id_z 0
		.amdhsa_system_sgpr_workgroup_info 0
		.amdhsa_system_vgpr_workitem_id 0
		.amdhsa_next_free_vgpr 114
		.amdhsa_next_free_sgpr 27
		.amdhsa_accum_offset 116
		.amdhsa_reserve_vcc 1
		.amdhsa_float_round_mode_32 0
		.amdhsa_float_round_mode_16_64 0
		.amdhsa_float_denorm_mode_32 3
		.amdhsa_float_denorm_mode_16_64 3
		.amdhsa_dx10_clamp 1
		.amdhsa_ieee_mode 1
		.amdhsa_fp16_overflow 0
		.amdhsa_tg_split 0
		.amdhsa_exception_fp_ieee_invalid_op 0
		.amdhsa_exception_fp_denorm_src 0
		.amdhsa_exception_fp_ieee_div_zero 0
		.amdhsa_exception_fp_ieee_overflow 0
		.amdhsa_exception_fp_ieee_underflow 0
		.amdhsa_exception_fp_ieee_inexact 0
		.amdhsa_exception_int_div_zero 0
	.end_amdhsa_kernel
